# ALiBi A-operand build: the redundant mask of the byte-to-float conversion (low 16 bits already zero) removed in the attention sub-tiles
# baseline (speedup 1.0000x reference)
.LBB0_447:
	s_add_i32 s2, s26, s23
	s_and_b32 s3, s30, 0x18000
	s_add_i32 s3, s3, 0
	s_add_i32 s33, s3, s27
	v_add_u32_e32 v2, s33, v162
	v_add_u32_e32 v4, s33, v164
	v_add_u32_e32 v5, s33, v165
	v_add_u32_e32 v70, s33, v166
	s_ashr_i32 s33, s31, 2
	v_cvt_f32_i32_e32 v170, s33
	v_add_u32_e32 v106, s3, v160
	s_add_i32 s3, s2, 0x7e0
	v_add_u32_e32 v169, 0x4000, v106
	s_cmp_gt_i32 s3, s28
	v_add_u32_e32 v174, v2, v145
	v_add_u32_e32 v173, v4, v145
	v_add_u32_e32 v172, v5, v145
	v_add_u32_e32 v171, v70, v145
	s_barrier
	s_cbranch_scc1 .LBB0_455
	ds_read_b128 v[70:73], v174 offset:4096
	ds_read_b128 v[188:191], v173 offset:4096
	ds_read_b128 v[192:195], v172 offset:4096
	ds_read_b128 v[202:205], v171 offset:4096
	s_and_b32 s3, s3, 0xe0
	v_or_b32_e32 v2, s3, v159
	v_cvt_f32_ubyte0_e32 v2, v2
	v_or_b32_sdwa v2, v2, v170 dst_sel:DWORD dst_unused:UNUSED_PAD src0_sel:DWORD src1_sel:WORD_1
	v_cndmask_b32_e64 v2, 0, v2, s[36:37]
	v_mov_b32_e32 v4, v3
	s_waitcnt lgkmcnt(3)
	s_setprio 1
	v_mfma_f32_32x32x16_bf16 v[70:85], v[70:73], v[86:89], 0
	v_mov_b32_e32 v5, v3
	s_add_i32 s3, s2, 0x7ff
	s_cmp_ge_i32 s19, s3
	s_cselect_b64 s[40:41], -1, 0
	s_add_i32 s3, s29, 0xffffffa0
	s_cmp_lt_i32 s3, 0x3fffffe1
	v_add_u32_e32 v175, v169, v150
	s_waitcnt lgkmcnt(2)
	v_mfma_f32_32x32x16_bf16 v[70:85], v[188:191], v[90:93], v[70:85]
	s_cselect_b64 s[42:43], -1, 0
	s_and_b64 s[40:41], s[40:41], s[42:43]
	s_and_b64 vcc, exec, s[40:41]
	s_waitcnt lgkmcnt(1)
	v_mfma_f32_32x32x16_bf16 v[70:85], v[192:195], v[94:97], v[70:85]
	s_waitcnt lgkmcnt(0)
	v_mfma_f32_32x32x16_bf16 v[70:85], v[202:205], v[98:101], v[70:85]
	v_mfma_f32_32x32x16_bf16 v[70:85], v[2:5], v[102:105], v[70:85]
	v_add3_u32 v2, v106, v142, s68
	v_add_u32_e32 v4, v169, v146
	v_add_u32_e32 v5, v169, v148
	ds_read_b64_tr_b16 v[134:135], v2
	ds_read_b64_tr_b16 v[136:137], v2 offset:2048
	ds_read_b64_tr_b16 v[130:131], v4
	ds_read_b64_tr_b16 v[132:133], v4 offset:2048
	ds_read_b64_tr_b16 v[126:127], v5
	ds_read_b64_tr_b16 v[128:129], v5 offset:2048
	ds_read_b64_tr_b16 v[122:123], v175
	ds_read_b64_tr_b16 v[124:125], v175 offset:2048
	ds_read_b64_tr_b16 v[118:119], v2 offset:4096
	ds_read_b64_tr_b16 v[120:121], v2 offset:6144
	ds_read_b64_tr_b16 v[114:115], v4 offset:4096
	ds_read_b64_tr_b16 v[116:117], v4 offset:6144
	ds_read_b64_tr_b16 v[110:111], v5 offset:4096
	ds_read_b64_tr_b16 v[112:113], v5 offset:6144
	ds_read_b64_tr_b16 v[106:107], v175 offset:4096
	ds_read_b64_tr_b16 v[108:109], v175 offset:6144
	s_cbranch_vccnz .LBB0_452
	v_add_u32_e32 v2, s29, v161
	v_add_u32_e32 v4, 0xffffffa0, v2
	v_cmp_gt_u32_e32 vcc, 2.0, v4
	v_add_u32_e32 v4, s23, v163
	v_add_u32_e32 v4, 0x60, v4
	s_nop 2
	v_cndmask_b32_e32 v70, v197, v70, vcc
	v_cmp_lt_u32_e32 vcc, s75, v4
	v_add_u32_e32 v4, 0xffffff9e, v2
	s_nop 0
	v_cndmask_b32_e32 v71, v197, v71, vcc
	v_cmp_gt_u32_e32 vcc, 2.0, v4
	v_add_u32_e32 v4, 0xffffff9d, v2
	s_nop 0
	v_cndmask_b32_e32 v72, v197, v72, vcc
	v_cmp_gt_u32_e32 vcc, 2.0, v4
	v_add_u32_e32 v4, 0xffffff98, v2
	s_nop 0
	v_cndmask_b32_e32 v73, v197, v73, vcc
	v_cmp_gt_u32_e32 vcc, 2.0, v4
	v_add_u32_e32 v4, 0xffffff97, v2
	s_nop 0
	v_cndmask_b32_e32 v74, v197, v74, vcc
	v_cmp_gt_u32_e32 vcc, 2.0, v4
	v_add_u32_e32 v4, 0xffffff96, v2
	s_nop 0
	v_cndmask_b32_e32 v75, v197, v75, vcc
	v_cmp_gt_u32_e32 vcc, 2.0, v4
	v_add_u32_e32 v4, 0xffffff95, v2
	s_nop 0
	v_cndmask_b32_e32 v76, v197, v76, vcc
	v_cmp_gt_u32_e32 vcc, 2.0, v4
	v_add_u32_e32 v4, 0xffffff90, v2
	s_nop 0
	v_cndmask_b32_e32 v77, v197, v77, vcc
	v_cmp_gt_u32_e32 vcc, 2.0, v4
	v_add_u32_e32 v4, 0xffffff8f, v2
	s_nop 0
	v_cndmask_b32_e32 v78, v197, v78, vcc
	v_cmp_gt_u32_e32 vcc, 2.0, v4
	v_add_u32_e32 v4, 0xffffff8e, v2
	s_nop 0
	v_cndmask_b32_e32 v79, v197, v79, vcc
	v_cmp_gt_u32_e32 vcc, 2.0, v4
	v_add_u32_e32 v4, 0xffffff8d, v2
	s_nop 0
	v_cndmask_b32_e32 v80, v197, v80, vcc
	v_cmp_gt_u32_e32 vcc, 2.0, v4
	v_add_u32_e32 v4, 0xffffff88, v2
	s_nop 0
	v_cndmask_b32_e32 v81, v197, v81, vcc
	v_cmp_gt_u32_e32 vcc, 2.0, v4
	v_add_u32_e32 v4, 0xffffff87, v2
	s_nop 0
	v_cndmask_b32_e32 v82, v197, v82, vcc
	v_cmp_gt_u32_e32 vcc, 2.0, v4
	v_add_u32_e32 v4, 0xffffff86, v2
	v_add_u32_e32 v2, 0xffffff85, v2
	v_cndmask_b32_e32 v83, v197, v83, vcc
	v_cmp_gt_u32_e32 vcc, 2.0, v4
	s_nop 1
	v_cndmask_b32_e32 v84, v197, v84, vcc
	v_cmp_gt_u32_e32 vcc, 2.0, v2
	s_nop 1
	v_cndmask_b32_e32 v85, v197, v85, vcc

.Lring_issue_skip_2:
	s_add_i32 s3, s2, 0x7c0
	s_cmp_gt_i32 s3, s28
	s_cbranch_scc1 .LBB0_461
	ds_read_b128 v[70:73], v174
	ds_read_b128 v[188:191], v173
	ds_read_b128 v[192:195], v172
	ds_read_b128 v[202:205], v171
	s_and_b32 s3, s3, 0xc0
	v_or_b32_e32 v2, s3, v159
	v_cvt_f32_ubyte0_e32 v2, v2
	v_or_b32_sdwa v2, v2, v170 dst_sel:DWORD dst_unused:UNUSED_PAD src0_sel:DWORD src1_sel:WORD_1
	v_cndmask_b32_e64 v2, 0, v2, s[36:37]
	v_mov_b32_e32 v4, v3
	s_waitcnt lgkmcnt(3)
	s_setprio 1
	v_mfma_f32_32x32x16_bf16 v[70:85], v[70:73], v[86:89], 0
	v_mov_b32_e32 v5, v3
	s_addk_i32 s2, 0x7df
	s_cmp_ge_i32 s19, s2
	s_cselect_b64 s[2:3], -1, 0
	s_sub_i32 s33, s29, 64
	s_cmp_lt_i32 s33, 0x3fffffe1
	s_cselect_b64 s[40:41], -1, 0
	s_waitcnt lgkmcnt(2)
	v_mfma_f32_32x32x16_bf16 v[70:85], v[188:191], v[90:93], v[70:85]
	s_and_b64 s[2:3], s[2:3], s[40:41]
	s_and_b64 vcc, exec, s[2:3]
	s_waitcnt lgkmcnt(1)
	v_mfma_f32_32x32x16_bf16 v[70:85], v[192:195], v[94:97], v[70:85]
	s_waitcnt lgkmcnt(0)
	v_mfma_f32_32x32x16_bf16 v[70:85], v[202:205], v[98:101], v[70:85]
	v_mfma_f32_32x32x16_bf16 v[70:85], v[2:5], v[102:105], v[70:85]
	v_add_u32_e32 v2, v169, v142
	v_add_u32_e32 v4, v169, v152
	v_add_u32_e32 v5, v169, v154
	v_add_u32_e32 v169, v169, v156
	ds_read_b64_tr_b16 v[134:135], v2
	ds_read_b64_tr_b16 v[136:137], v2 offset:2048
	ds_read_b64_tr_b16 v[130:131], v4
	ds_read_b64_tr_b16 v[132:133], v4 offset:2048
	ds_read_b64_tr_b16 v[126:127], v5
	ds_read_b64_tr_b16 v[128:129], v5 offset:2048
	ds_read_b64_tr_b16 v[122:123], v169
	ds_read_b64_tr_b16 v[124:125], v169 offset:2048
	ds_read_b64_tr_b16 v[118:119], v2 offset:4096
	ds_read_b64_tr_b16 v[120:121], v2 offset:6144
	ds_read_b64_tr_b16 v[114:115], v4 offset:4096
	ds_read_b64_tr_b16 v[116:117], v4 offset:6144
	ds_read_b64_tr_b16 v[110:111], v5 offset:4096
	ds_read_b64_tr_b16 v[112:113], v5 offset:6144
	ds_read_b64_tr_b16 v[106:107], v169 offset:4096
	ds_read_b64_tr_b16 v[108:109], v169 offset:6144
	s_cbranch_vccnz .LBB0_458
	v_add_u32_e32 v2, s29, v161
	v_subrev_u32_e32 v4, 64, v2
	v_cmp_gt_u32_e32 vcc, 2.0, v4
	v_add3_u32 v4, v163, s23, 64
	s_nop 2
	v_cndmask_b32_e32 v70, v197, v70, vcc
	v_cmp_lt_u32_e32 vcc, s75, v4
	v_add_u32_e32 v4, 0xffffffbe, v2
	s_nop 0
	v_cndmask_b32_e32 v71, v197, v71, vcc
	v_cmp_gt_u32_e32 vcc, 2.0, v4
	v_add_u32_e32 v4, 0xffffffbd, v2
	s_nop 0
	v_cndmask_b32_e32 v72, v197, v72, vcc
	v_cmp_gt_u32_e32 vcc, 2.0, v4
	v_add_u32_e32 v4, 0xffffffb8, v2
	s_nop 0
	v_cndmask_b32_e32 v73, v197, v73, vcc
	v_cmp_gt_u32_e32 vcc, 2.0, v4
	v_add_u32_e32 v4, 0xffffffb7, v2
	s_nop 0
	v_cndmask_b32_e32 v74, v197, v74, vcc
	v_cmp_gt_u32_e32 vcc, 2.0, v4
	v_add_u32_e32 v4, 0xffffffb6, v2
	s_nop 0
	v_cndmask_b32_e32 v75, v197, v75, vcc
	v_cmp_gt_u32_e32 vcc, 2.0, v4
	v_add_u32_e32 v4, 0xffffffb5, v2
	s_nop 0
	v_cndmask_b32_e32 v76, v197, v76, vcc
	v_cmp_gt_u32_e32 vcc, 2.0, v4
	v_add_u32_e32 v4, 0xffffffb0, v2
	s_nop 0
	v_cndmask_b32_e32 v77, v197, v77, vcc
	v_cmp_gt_u32_e32 vcc, 2.0, v4
	v_add_u32_e32 v4, 0xffffffaf, v2
	s_nop 0
	v_cndmask_b32_e32 v78, v197, v78, vcc
	v_cmp_gt_u32_e32 vcc, 2.0, v4
	v_add_u32_e32 v4, 0xffffffae, v2
	s_nop 0
	v_cndmask_b32_e32 v79, v197, v79, vcc
	v_cmp_gt_u32_e32 vcc, 2.0, v4
	v_add_u32_e32 v4, 0xffffffad, v2
	s_nop 0
	v_cndmask_b32_e32 v80, v197, v80, vcc
	v_cmp_gt_u32_e32 vcc, 2.0, v4
	v_add_u32_e32 v4, 0xffffffa8, v2
	s_nop 0
	v_cndmask_b32_e32 v81, v197, v81, vcc
	v_cmp_gt_u32_e32 vcc, 2.0, v4
	v_add_u32_e32 v4, 0xffffffa7, v2
	s_nop 0
	v_cndmask_b32_e32 v82, v197, v82, vcc
	v_cmp_gt_u32_e32 vcc, 2.0, v4
	v_add_u32_e32 v4, 0xffffffa6, v2
	v_add_u32_e32 v2, 0xffffffa5, v2
	v_cndmask_b32_e32 v83, v197, v83, vcc
	v_cmp_gt_u32_e32 vcc, 2.0, v4
	s_nop 1
	v_cndmask_b32_e32 v84, v197, v84, vcc
	v_cmp_gt_u32_e32 vcc, 2.0, v2
	s_nop 1
	v_cndmask_b32_e32 v85, v197, v85, vcc

.Lw_win_4_done:
.LBB0_519:
	s_cmp_eq_u32 s32, 0
	s_cselect_b32 s84, 0, 1
	s_sub_u32 s32, s32, s84
	s_add_i32 s2, s29, s22
	s_add_i32 s3, s27, s21
	s_add_i32 s3, s3, -1
	s_and_b32 s31, s30, 0xc000
	s_add_i32 s33, s31, 0
	s_ashr_i32 s3, s3, 2
	s_add_i32 s31, s2, 0x7e0
	s_cmp_gt_i32 s31, s23
	v_cvt_f32_i32_e32 v111, s3
	s_cselect_b64 s[34:35], -1, 0
	s_add_i32 s3, s2, 0x7ff
	s_cmp_lt_i32 s3, s24
	s_cselect_b64 s[38:39], -1, 0
	v_add_u32_e32 v2, s33, v101
	v_add_u32_e32 v4, s33, v102
	v_add_u32_e32 v5, s33, v103
	v_add_u32_e32 v6, s33, v104
	s_or_b64 s[34:35], s[34:35], s[38:39]
	s_and_b64 vcc, exec, s[34:35]
	v_add_u32_e32 v115, v2, v100
	v_add_u32_e32 v114, v4, v100
	v_add_u32_e32 v113, v5, v100
	v_add_u32_e32 v112, v6, v100
	v_add_u32_e32 v16, s33, v105
	v_add_u32_e32 v17, s33, v106
	s_barrier
	s_cbranch_vccnz .LBB0_527
	ds_read_b128 v[4:7], v115 offset:4096
	ds_read_b128 v[188:191], v114 offset:4096
	ds_read_b128 v[192:195], v113 offset:4096
	ds_read_b128 v[202:205], v112 offset:4096
	s_and_b32 s31, s31, 0xe0
	v_or_b32_e32 v2, s31, v99
	v_cvt_f32_ubyte0_e32 v2, v2
	v_or_b32_sdwa v2, v2, v111 dst_sel:DWORD dst_unused:UNUSED_PAD src0_sel:DWORD src1_sel:WORD_1
	v_cndmask_b32_e64 v246, 0, v2, s[36:37]
	s_cmp_ge_i32 s20, s3
	s_cselect_b64 s[34:35], -1, 0
	s_waitcnt lgkmcnt(3)
	s_setprio 1
	v_mfma_f32_32x32x16_bf16 v[50:65], v[4:7], v[74:77], 0
	s_sub_i32 s3, s19, 32
	s_cmpk_lt_i32 s3, 0x1e1
	v_add3_u32 v116, v17, v94, s69
	s_cselect_b64 s[38:39], -1, 0
	s_and_b64 s[34:35], s[34:35], s[38:39]
	s_and_b64 vcc, exec, s[34:35]
	s_waitcnt lgkmcnt(2)
	v_mfma_f32_32x32x16_bf16 v[50:65], v[188:191], v[66:69], v[50:65]
	s_waitcnt lgkmcnt(1)
	v_mfma_f32_32x32x16_bf16 v[50:65], v[192:195], v[70:73], v[50:65]
	s_waitcnt lgkmcnt(0)
	v_mfma_f32_32x32x16_bf16 v[50:65], v[202:205], v[78:81], v[50:65]
	v_mfma_f32_32x32x16_bf16 v[50:65], v[246:249], v[82:85], v[50:65]
	v_add3_u32 v2, v16, v94, s69
	ds_read_b64_tr_b16 v[86:87], v2
	ds_read_b64_tr_b16 v[88:89], v2 offset:1024
	ds_read_b64_tr_b16 v[12:13], v116
	ds_read_b64_tr_b16 v[14:15], v116 offset:1024
	ds_read_b64_tr_b16 v[8:9], v2 offset:2048
	ds_read_b64_tr_b16 v[10:11], v2 offset:3072
	ds_read_b64_tr_b16 v[4:5], v116 offset:2048
	ds_read_b64_tr_b16 v[6:7], v116 offset:3072
	s_cbranch_vccnz .LBB0_524
	v_add_u32_e32 v2, s19, v108
	v_subrev_u32_e32 v116, 32, v2
	v_cmp_gt_u32_e32 vcc, s79, v116
	v_add3_u32 v116, v109, s22, 32
	s_nop 5
	v_cndmask_b32_e32 v50, v197, v50, vcc
	v_cmp_lt_u32_e32 vcc, s80, v116
	v_subrev_u32_e32 v116, 34, v2
	s_nop 0
	v_cndmask_b32_e32 v51, v197, v51, vcc
	v_cmp_gt_u32_e32 vcc, s79, v116
	v_subrev_u32_e32 v116, 35, v2
	s_nop 0
	v_cndmask_b32_e32 v52, v197, v52, vcc
	v_cmp_gt_u32_e32 vcc, s79, v116
	v_subrev_u32_e32 v116, 40, v2
	s_nop 0
	v_cndmask_b32_e32 v53, v197, v53, vcc
	v_cmp_gt_u32_e32 vcc, s79, v116
	v_subrev_u32_e32 v116, 41, v2
	s_nop 0
	v_cndmask_b32_e32 v54, v197, v54, vcc
	v_cmp_gt_u32_e32 vcc, s79, v116
	v_subrev_u32_e32 v116, 42, v2
	s_nop 0
	v_cndmask_b32_e32 v55, v197, v55, vcc
	v_cmp_gt_u32_e32 vcc, s79, v116
	v_subrev_u32_e32 v116, 43, v2
	s_nop 0
	v_cndmask_b32_e32 v56, v197, v56, vcc
	v_cmp_gt_u32_e32 vcc, s79, v116
	v_subrev_u32_e32 v116, 48, v2
	s_nop 0
	v_cndmask_b32_e32 v57, v197, v57, vcc
	v_cmp_gt_u32_e32 vcc, s79, v116
	v_subrev_u32_e32 v116, 49, v2
	s_nop 0
	v_cndmask_b32_e32 v58, v197, v58, vcc
	v_cmp_gt_u32_e32 vcc, s79, v116
	v_subrev_u32_e32 v116, 50, v2
	s_nop 0
	v_cndmask_b32_e32 v59, v197, v59, vcc
	v_cmp_gt_u32_e32 vcc, s79, v116
	v_subrev_u32_e32 v116, 51, v2
	s_nop 0
	v_cndmask_b32_e32 v60, v197, v60, vcc
	v_cmp_gt_u32_e32 vcc, s79, v116
	v_subrev_u32_e32 v116, 56, v2
	s_nop 0
	v_cndmask_b32_e32 v61, v197, v61, vcc
	v_cmp_gt_u32_e32 vcc, s79, v116
	v_subrev_u32_e32 v116, 57, v2
	s_nop 0
	v_cndmask_b32_e32 v62, v197, v62, vcc
	v_cmp_gt_u32_e32 vcc, s79, v116
	v_subrev_u32_e32 v116, 58, v2
	v_subrev_u32_e32 v2, 59, v2
	v_cndmask_b32_e32 v63, v197, v63, vcc
	v_cmp_gt_u32_e32 vcc, s79, v116
	s_nop 1
	v_cndmask_b32_e32 v64, v197, v64, vcc
	v_cmp_gt_u32_e32 vcc, s79, v2
	s_nop 1
	v_cndmask_b32_e32 v65, v197, v65, vcc

.Lring_issue_skip_0:
	s_add_i32 s3, s2, 0x7c0
	s_cmp_gt_i32 s3, s23
	s_cselect_b64 s[34:35], -1, 0
	s_addk_i32 s2, 0x7df
	s_cmp_lt_i32 s2, s24
	s_cselect_b64 s[38:39], -1, 0
	s_or_b64 s[34:35], s[34:35], s[38:39]
	s_and_b64 vcc, exec, s[34:35]
	s_cbranch_vccnz .LBB0_510
	ds_read_b128 v[4:7], v115
	ds_read_b128 v[188:191], v114
	ds_read_b128 v[192:195], v113
	ds_read_b128 v[202:205], v112
	s_and_b32 s3, s3, 0xc0
	v_or_b32_e32 v2, s3, v99
	v_cvt_f32_ubyte0_e32 v2, v2
	v_or_b32_sdwa v2, v2, v111 dst_sel:DWORD dst_unused:UNUSED_PAD src0_sel:DWORD src1_sel:WORD_1
	v_cndmask_b32_e64 v246, 0, v2, s[36:37]
	s_cmp_ge_i32 s20, s2
	s_cselect_b64 s[2:3], -1, 0
	s_waitcnt lgkmcnt(3)
	s_setprio 1
	v_mfma_f32_32x32x16_bf16 v[50:65], v[4:7], v[74:77], 0
	s_cmpk_lt_i32 s19, 0x1e1
	s_cselect_b64 s[34:35], -1, 0
	s_and_b64 s[2:3], s[2:3], s[34:35]
	s_and_b64 vcc, exec, s[2:3]
	s_waitcnt lgkmcnt(2)
	v_mfma_f32_32x32x16_bf16 v[50:65], v[188:191], v[66:69], v[50:65]
	s_waitcnt lgkmcnt(1)
	v_mfma_f32_32x32x16_bf16 v[50:65], v[192:195], v[70:73], v[50:65]
	s_waitcnt lgkmcnt(0)
	v_mfma_f32_32x32x16_bf16 v[50:65], v[202:205], v[78:81], v[50:65]
	v_mfma_f32_32x32x16_bf16 v[50:65], v[246:249], v[82:85], v[50:65]
	v_add3_u32 v2, v16, v94, s67
	v_add3_u32 v16, v17, v94, s67
	ds_read_b64_tr_b16 v[86:87], v2
	ds_read_b64_tr_b16 v[88:89], v2 offset:1024
	ds_read_b64_tr_b16 v[12:13], v16
	ds_read_b64_tr_b16 v[14:15], v16 offset:1024
	ds_read_b64_tr_b16 v[8:9], v2 offset:2048
	ds_read_b64_tr_b16 v[10:11], v2 offset:3072
	ds_read_b64_tr_b16 v[4:5], v16 offset:2048
	ds_read_b64_tr_b16 v[6:7], v16 offset:3072
	s_cbranch_vccnz .LBB0_530
	v_add_u32_e32 v2, s19, v108
	v_cmp_gt_u32_e32 vcc, s79, v2
	v_add_u32_e32 v16, s22, v109
	s_nop 5
	v_cndmask_b32_e32 v50, v197, v50, vcc
	v_cmp_lt_u32_e32 vcc, s80, v16
	v_add_u32_e32 v16, -2, v2
	s_nop 0
	v_cndmask_b32_e32 v51, v197, v51, vcc
	v_cmp_gt_u32_e32 vcc, s79, v16
	v_add_u32_e32 v16, -3, v2
	s_nop 0
	v_cndmask_b32_e32 v52, v197, v52, vcc
	v_cmp_gt_u32_e32 vcc, s79, v16
	v_add_u32_e32 v16, -8, v2
	s_nop 0
	v_cndmask_b32_e32 v53, v197, v53, vcc
	v_cmp_gt_u32_e32 vcc, s79, v16
	v_add_u32_e32 v16, -9, v2
	s_nop 0
	v_cndmask_b32_e32 v54, v197, v54, vcc
	v_cmp_gt_u32_e32 vcc, s79, v16
	v_add_u32_e32 v16, -10, v2
	s_nop 0
	v_cndmask_b32_e32 v55, v197, v55, vcc
	v_cmp_gt_u32_e32 vcc, s79, v16
	v_add_u32_e32 v16, -11, v2
	s_nop 0
	v_cndmask_b32_e32 v56, v197, v56, vcc
	v_cmp_gt_u32_e32 vcc, s79, v16
	v_add_u32_e32 v16, -16, v2
	s_nop 0
	v_cndmask_b32_e32 v57, v197, v57, vcc
	v_cmp_gt_u32_e32 vcc, s79, v16
	v_subrev_u32_e32 v16, 17, v2
	s_nop 0
	v_cndmask_b32_e32 v58, v197, v58, vcc
	v_cmp_gt_u32_e32 vcc, s79, v16
	v_subrev_u32_e32 v16, 18, v2
	s_nop 0
	v_cndmask_b32_e32 v59, v197, v59, vcc
	v_cmp_gt_u32_e32 vcc, s79, v16
	v_subrev_u32_e32 v16, 19, v2
	s_nop 0
	v_cndmask_b32_e32 v60, v197, v60, vcc
	v_cmp_gt_u32_e32 vcc, s79, v16
	v_subrev_u32_e32 v16, 24, v2
	s_nop 0
	v_cndmask_b32_e32 v61, v197, v61, vcc
	v_cmp_gt_u32_e32 vcc, s79, v16
	v_subrev_u32_e32 v16, 25, v2
	s_nop 0
	v_cndmask_b32_e32 v62, v197, v62, vcc
	v_cmp_gt_u32_e32 vcc, s79, v16
	v_subrev_u32_e32 v16, 26, v2
	v_subrev_u32_e32 v2, 27, v2
	v_cndmask_b32_e32 v63, v197, v63, vcc
	v_cmp_gt_u32_e32 vcc, s79, v16
	s_nop 1
	v_cndmask_b32_e32 v64, v197, v64, vcc
	v_cmp_gt_u32_e32 vcc, s79, v2
	s_nop 1
	v_cndmask_b32_e32 v65, v197, v65, vcc

.LBB0_666:
	s_cmp_eq_u32 s2, 0
	.p2align 8
	s_cbranch_scc1 .LBB0_697
	s_add_i32 s0, s15, 1
	v_cvt_f32_ubyte0_e32 v2, s0
	s_mov_b32 s0, 0x42fc0000
	v_cmp_lt_f32_e32 vcc, s0, v2
	v_mov_b32_e32 v11, 0x42800000
	s_and_b64 s[0:1], vcc, exec
	v_cndmask_b32_e32 v11, 0, v11, vcc
	v_sub_f32_e32 v2, v11, v2
	v_exp_f32_e32 v2, v2
	s_cselect_b32 s0, 0xffffffc0, 0
	v_mov_b32_e32 v16, v3
	v_mov_b32_e32 v17, v3
	v_ldexp_f32 v2, v2, s0
	v_mul_f32_e32 v11, 0x43800000, v2
	v_or_b32_sdwa v2, v11, v2 dst_sel:DWORD dst_unused:UNUSED_PAD src0_sel:WORD_1 src1_sel:DWORD
	v_cndmask_b32_e64 v114, 0, v2, s[22:23]
	v_bitop3_b32 v2, v67, v6, 15 bitop3:0x78
	v_lshlrev_b32_e32 v137, 4, v2
	v_bitop3_b32 v2, v10, v6, 15 bitop3:0x78
	v_lshlrev_b32_e32 v138, 4, v2
	v_bitop3_b32 v2, v9, v6, 15 bitop3:0x78
	v_lshlrev_b32_e32 v139, 4, v2
	v_bitop3_b32 v2, v8, v6, 15 bitop3:0x78
	v_lshlrev_b32_e32 v140, 4, v2
	v_and_or_b32 v2, v6, 1, v5
	v_lshl_or_b32 v2, v2, 4, v7
	v_or_b32_e32 v156, v2, v4
	v_bitop3_b32 v157, v2, 64, v4 bitop3:0x36
	v_mov_b32_e32 v2, v3
	v_mov_b32_e32 v4, v3
	v_mov_b32_e32 v5, v3
	v_mov_b32_e32 v6, v3
	v_mov_b32_e32 v7, v3
	v_mov_b32_e32 v8, v3
	v_mov_b32_e32 v9, v3
	v_mov_b32_e32 v10, v3
	v_mov_b32_e32 v11, v3
	v_mov_b32_e32 v12, v3
	v_mov_b32_e32 v13, v3
	v_mov_b32_e32 v14, v3
	v_mov_b32_e32 v15, v3
	v_mov_b64_e32 v[80:81], v[16:17]
	v_mov_b64_e32 v[64:65], v[16:17]
	s_mov_b32 s5, 0
	v_mov_b32_e32 v115, v3
	v_mov_b32_e32 v116, v3
	v_mov_b32_e32 v117, v3
	s_or_b32 s6, s16, 31
	v_add_u32_e32 v141, -2, v126
	v_add_u32_e32 v142, -3, v126
	v_add_u32_e32 v143, -8, v126
	v_add_u32_e32 v145, -9, v126
	v_add_u32_e32 v146, -10, v126
	v_add_u32_e32 v147, -11, v126
	v_add_u32_e32 v148, -16, v126
	v_subrev_u32_e32 v149, 17, v126
	v_subrev_u32_e32 v150, 18, v126
	v_subrev_u32_e32 v151, 19, v126
	v_subrev_u32_e32 v152, 24, v126
	v_subrev_u32_e32 v153, 25, v126
	v_subrev_u32_e32 v154, 26, v126
	v_subrev_u32_e32 v155, 27, v126
	v_mov_b32_e32 v144, 0
	v_mov_b32_e32 v158, 0xf149f2ca
	s_mov_b32 s7, -1
	v_mov_b64_e32 v[78:79], v[14:15]
	v_mov_b64_e32 v[76:77], v[12:13]
	v_mov_b64_e32 v[74:75], v[10:11]
	v_mov_b64_e32 v[72:73], v[8:9]
	v_mov_b64_e32 v[70:71], v[6:7]
	v_mov_b64_e32 v[68:69], v[4:5]
	v_mov_b64_e32 v[66:67], v[2:3]
	v_mov_b64_e32 v[62:63], v[14:15]
	v_mov_b64_e32 v[60:61], v[12:13]
	v_mov_b64_e32 v[58:59], v[10:11]
	v_mov_b64_e32 v[56:57], v[8:9]
	v_mov_b64_e32 v[54:55], v[6:7]
	v_mov_b64_e32 v[52:53], v[4:5]
	v_mov_b64_e32 v[50:51], v[2:3]
	s_branch .LBB0_670

.LBB0_681:
	s_flbit_i32_b32 s0, s2
	s_xor_b32 s0, s0, 31
	s_lshl_b32 s8, 1, s0
	s_waitcnt lgkmcnt(0)
	v_and_b32_e32 v2, s8, v136
	v_cmp_ne_u32_e64 s[38:39], 0, v2
	s_mov_b64 vcc, s[38:39]
	s_cbranch_vccz .LBB0_669
	s_and_b32 s1, s5, 0xc000
	s_lshl_b32 s9, s0, 6
	s_lshr_b32 s0, s0, 2
	s_xor_b32 s1, s1, 0x8000
	v_cvt_f32_u32_e32 v159, s0
	s_add_i32 s1, s1, 0
	v_add_u32_e32 v2, s1, v137
	v_add_u32_e32 v4, s1, v138
	v_add_u32_e32 v5, s1, v139
	v_add_u32_e32 v6, s1, v140
	s_or_b32 s10, s9, 32
	s_cmp_gt_i32 s10, s6
	v_add_u32_e32 v163, v2, v134
	v_add_u32_e32 v162, v4, v134
	v_add_u32_e32 v161, v5, v134
	v_add_u32_e32 v160, v6, v134
	v_add_u32_e32 v17, s1, v156
	v_add_u32_e32 v16, s1, v157
	s_cbranch_scc1 .LBB0_690
	ds_read_b128 v[4:7], v163 offset:4096
	ds_read_b128 v[188:191], v162 offset:4096
	ds_read_b128 v[192:195], v161 offset:4096
	ds_read_b128 v[202:205], v160 offset:4096
	s_and_b32 s0, s10, 0xe0
	v_or_b32_e32 v2, s0, v129
	v_cvt_f32_ubyte0_e32 v2, v2
	v_or_b32_sdwa v2, v2, v159 dst_sel:DWORD dst_unused:UNUSED_PAD src0_sel:DWORD src1_sel:WORD_1
	v_cndmask_b32_e64 v210, 0, v2, s[22:23]
	s_or_b32 s0, s9, 63
	s_cmp_lt_u32 s16, s0
	s_waitcnt lgkmcnt(3)
	s_setprio 1
	v_mfma_f32_32x32x16_bf16 v[82:97], v[4:7], v[106:109], 0
	s_cselect_b64 s[0:1], -1, 0
	s_sub_i32 s11, s16, s10
	s_cmp_gt_i32 s11, 0x3fffffe0
	v_add3_u32 v164, v16, v135, s69
	s_cselect_b64 s[12:13], -1, 0
	s_or_b64 s[0:1], s[0:1], s[12:13]
	s_and_b64 vcc, exec, s[0:1]
	s_waitcnt lgkmcnt(2)
	v_mfma_f32_32x32x16_bf16 v[82:97], v[188:191], v[98:101], v[82:97]
	s_waitcnt lgkmcnt(1)
	v_mfma_f32_32x32x16_bf16 v[82:97], v[192:195], v[102:105], v[82:97]
	s_waitcnt lgkmcnt(0)
	v_mfma_f32_32x32x16_bf16 v[82:97], v[202:205], v[110:113], v[82:97]
	v_mfma_f32_32x32x16_bf16 v[82:97], v[210:213], v[114:117], v[82:97]
	v_add3_u32 v2, v17, v135, s69
	ds_read_b64_tr_b16 v[118:119], v2
	ds_read_b64_tr_b16 v[120:121], v2 offset:1024
	ds_read_b64_tr_b16 v[12:13], v164
	ds_read_b64_tr_b16 v[14:15], v164 offset:1024
	ds_read_b64_tr_b16 v[8:9], v2 offset:2048
	ds_read_b64_tr_b16 v[10:11], v2 offset:3072
	ds_read_b64_tr_b16 v[4:5], v164 offset:2048
	ds_read_b64_tr_b16 v[6:7], v164 offset:3072
	s_cbranch_vccnz .LBB0_685
	v_cndmask_b32_e64 v2, 0, 1, s[38:39]
	v_cmp_ne_u32_e32 vcc, 0, v2
	s_cmp_lg_u64 vcc, exec
	s_cselect_b64 s[0:1], -1, 0
	s_cbranch_scc0 .LBB0_687
	v_cndmask_b32_e64 v82, v197, v82, s[38:39]
	v_cndmask_b32_e64 v83, v197, v83, s[38:39]
	v_cndmask_b32_e64 v84, v197, v84, s[38:39]
	v_cndmask_b32_e64 v85, v197, v85, s[38:39]
	v_cndmask_b32_e64 v86, v197, v86, s[38:39]
	v_cndmask_b32_e64 v87, v197, v87, s[38:39]
	v_cndmask_b32_e64 v88, v197, v88, s[38:39]
	v_cndmask_b32_e64 v89, v197, v89, s[38:39]
	v_cndmask_b32_e64 v90, v197, v90, s[38:39]
	v_cndmask_b32_e64 v91, v197, v91, s[38:39]
	v_cndmask_b32_e64 v92, v197, v92, s[38:39]
	v_cndmask_b32_e64 v93, v197, v93, s[38:39]
	v_cndmask_b32_e64 v94, v197, v94, s[38:39]
	v_cndmask_b32_e64 v95, v197, v95, s[38:39]
	v_cndmask_b32_e64 v96, v197, v96, s[38:39]
	v_cndmask_b32_e64 v97, v197, v97, s[38:39]
	s_branch .LBB0_687

.LBB0_690:
	s_cmp_gt_i32 s9, s6
	s_cbranch_scc1 .LBB0_669
	ds_read_b128 v[4:7], v163
	ds_read_b128 v[188:191], v162
	ds_read_b128 v[192:195], v161
	ds_read_b128 v[202:205], v160
	s_and_b32 s0, s9, 0xc0
	v_or_b32_e32 v2, s0, v129
	v_cvt_f32_ubyte0_e32 v2, v2
	v_or_b32_sdwa v2, v2, v159 dst_sel:DWORD dst_unused:UNUSED_PAD src0_sel:DWORD src1_sel:WORD_1
	v_cndmask_b32_e64 v210, 0, v2, s[22:23]
	s_or_b32 s0, s9, 31
	s_cmp_lt_i32 s16, s0
	s_waitcnt lgkmcnt(3)
	s_setprio 1
	v_mfma_f32_32x32x16_bf16 v[82:97], v[4:7], v[106:109], 0
	s_cselect_b64 s[0:1], -1, 0
	s_sub_i32 s10, s16, s9
	s_cmp_gt_i32 s10, 0x3fffffe0
	v_add3_u32 v16, v16, v135, s67
	s_cselect_b64 s[10:11], -1, 0
	s_or_b64 s[0:1], s[0:1], s[10:11]
	s_and_b64 vcc, exec, s[0:1]
	s_waitcnt lgkmcnt(2)
	v_mfma_f32_32x32x16_bf16 v[82:97], v[188:191], v[98:101], v[82:97]
	s_waitcnt lgkmcnt(1)
	v_mfma_f32_32x32x16_bf16 v[82:97], v[192:195], v[102:105], v[82:97]
	s_waitcnt lgkmcnt(0)
	v_mfma_f32_32x32x16_bf16 v[82:97], v[202:205], v[110:113], v[82:97]
	v_mfma_f32_32x32x16_bf16 v[82:97], v[210:213], v[114:117], v[82:97]
	v_add3_u32 v2, v17, v135, s67
	ds_read_b64_tr_b16 v[118:119], v2
	ds_read_b64_tr_b16 v[120:121], v2 offset:1024
	ds_read_b64_tr_b16 v[12:13], v16
	ds_read_b64_tr_b16 v[14:15], v16 offset:1024
	ds_read_b64_tr_b16 v[8:9], v2 offset:2048
	ds_read_b64_tr_b16 v[10:11], v2 offset:3072
	ds_read_b64_tr_b16 v[4:5], v16 offset:2048
	ds_read_b64_tr_b16 v[6:7], v16 offset:3072
	s_cbranch_vccnz .LBB0_693
	v_cndmask_b32_e64 v2, 0, 1, s[38:39]
	v_cmp_ne_u32_e32 vcc, 0, v2
	s_cmp_lg_u64 vcc, exec
	s_cselect_b64 s[0:1], -1, 0
	s_cbranch_scc0 .LBB0_695
	v_cndmask_b32_e64 v82, v197, v82, s[38:39]
	v_cndmask_b32_e64 v83, v197, v83, s[38:39]
	v_cndmask_b32_e64 v84, v197, v84, s[38:39]
	v_cndmask_b32_e64 v85, v197, v85, s[38:39]
	v_cndmask_b32_e64 v86, v197, v86, s[38:39]
	v_cndmask_b32_e64 v87, v197, v87, s[38:39]
	v_cndmask_b32_e64 v88, v197, v88, s[38:39]
	v_cndmask_b32_e64 v89, v197, v89, s[38:39]
	v_cndmask_b32_e64 v90, v197, v90, s[38:39]
	v_cndmask_b32_e64 v91, v197, v91, s[38:39]
	v_cndmask_b32_e64 v92, v197, v92, s[38:39]
	v_cndmask_b32_e64 v93, v197, v93, s[38:39]
	v_cndmask_b32_e64 v94, v197, v94, s[38:39]
	v_cndmask_b32_e64 v95, v197, v95, s[38:39]
	v_cndmask_b32_e64 v96, v197, v96, s[38:39]
	v_cndmask_b32_e64 v97, v197, v97, s[38:39]
	s_branch .LBB0_695

.Lw_swa_4_done:
.LBB0_780:
	s_cmp_eq_u32 s32, 0
	s_cselect_b32 s84, 0, 1
	s_sub_u32 s32, s32, s84
	s_add_i32 s0, s25, s17
	s_add_i32 s1, s23, s18
	s_add_i32 s1, s1, -1
	s_and_b32 s27, s26, 0xc000
	s_add_i32 s34, s27, 0
	s_ashr_i32 s1, s1, 2
	s_add_i32 s27, s0, 0x7e0
	s_cmp_gt_i32 s27, s19
	v_cvt_f32_i32_e32 v114, s1
	s_cselect_b64 s[28:29], -1, 0
	s_add_i32 s1, s0, 0x7ff
	s_cmp_lt_i32 s1, s20
	s_cselect_b64 s[30:31], -1, 0
	v_add_u32_e32 v2, s34, v104
	v_add_u32_e32 v4, s34, v105
	v_add_u32_e32 v5, s34, v106
	v_add_u32_e32 v6, s34, v107
	s_or_b64 s[28:29], s[28:29], s[30:31]
	s_and_b64 vcc, exec, s[28:29]
	v_add_u32_e32 v118, v2, v103
	v_add_u32_e32 v117, v4, v103
	v_add_u32_e32 v116, v5, v103
	v_add_u32_e32 v115, v6, v103
	v_add_u32_e32 v16, s34, v109
	v_add_u32_e32 v17, s34, v110
	s_barrier
	s_cbranch_vccnz .LBB0_788
	ds_read_b128 v[4:7], v118 offset:4096
	ds_read_b128 v[188:191], v117 offset:4096
	ds_read_b128 v[192:195], v116 offset:4096
	ds_read_b128 v[202:205], v115 offset:4096
	s_and_b32 s27, s27, 0xe0
	v_or_b32_e32 v2, s27, v102
	v_cvt_f32_ubyte0_e32 v2, v2
	v_or_b32_sdwa v2, v2, v114 dst_sel:DWORD dst_unused:UNUSED_PAD src0_sel:DWORD src1_sel:WORD_1
	v_cndmask_b32_e64 v246, 0, v2, s[36:37]
	s_cmp_ge_i32 s16, s1
	s_cselect_b64 s[28:29], -1, 0
	s_waitcnt lgkmcnt(3)
	s_setprio 1
	v_mfma_f32_32x32x16_bf16 v[50:65], v[4:7], v[66:69], 0
	s_sub_i32 s1, s15, 32
	s_cmpk_lt_i32 s1, 0x61
	v_add3_u32 v119, v17, v96, s69
	s_cselect_b64 s[30:31], -1, 0
	s_and_b64 s[28:29], s[28:29], s[30:31]
	s_and_b64 vcc, exec, s[28:29]
	s_waitcnt lgkmcnt(2)
	v_mfma_f32_32x32x16_bf16 v[50:65], v[188:191], v[70:73], v[50:65]
	s_waitcnt lgkmcnt(1)
	v_mfma_f32_32x32x16_bf16 v[50:65], v[192:195], v[74:77], v[50:65]
	s_waitcnt lgkmcnt(0)
	v_mfma_f32_32x32x16_bf16 v[50:65], v[202:205], v[78:81], v[50:65]
	v_mfma_f32_32x32x16_bf16 v[50:65], v[246:249], v[82:85], v[50:65]
	v_add3_u32 v2, v16, v96, s69
	ds_read_b64_tr_b16 v[86:87], v2
	ds_read_b64_tr_b16 v[88:89], v2 offset:1024
	ds_read_b64_tr_b16 v[12:13], v119
	ds_read_b64_tr_b16 v[14:15], v119 offset:1024
	ds_read_b64_tr_b16 v[8:9], v2 offset:2048
	ds_read_b64_tr_b16 v[10:11], v2 offset:3072
	ds_read_b64_tr_b16 v[4:5], v119 offset:2048
	ds_read_b64_tr_b16 v[6:7], v119 offset:3072
	s_cbranch_vccnz .LBB0_785
	v_add_u32_e32 v2, s15, v111
	v_subrev_u32_e32 v119, 32, v2
	v_cmp_gt_u32_e32 vcc, s71, v119
	v_add3_u32 v119, v112, s17, 32
	s_nop 5
	v_cndmask_b32_e32 v50, v197, v50, vcc
	v_cmp_lt_u32_e32 vcc, s47, v119
	v_subrev_u32_e32 v119, 34, v2
	s_nop 0
	v_cndmask_b32_e32 v51, v197, v51, vcc
	v_cmp_gt_u32_e32 vcc, s71, v119
	v_subrev_u32_e32 v119, 35, v2
	s_nop 0
	v_cndmask_b32_e32 v52, v197, v52, vcc
	v_cmp_gt_u32_e32 vcc, s71, v119
	v_subrev_u32_e32 v119, 40, v2
	s_nop 0
	v_cndmask_b32_e32 v53, v197, v53, vcc
	v_cmp_gt_u32_e32 vcc, s71, v119
	v_subrev_u32_e32 v119, 41, v2
	s_nop 0
	v_cndmask_b32_e32 v54, v197, v54, vcc
	v_cmp_gt_u32_e32 vcc, s71, v119
	v_subrev_u32_e32 v119, 42, v2
	s_nop 0
	v_cndmask_b32_e32 v55, v197, v55, vcc
	v_cmp_gt_u32_e32 vcc, s71, v119
	v_subrev_u32_e32 v119, 43, v2
	s_nop 0
	v_cndmask_b32_e32 v56, v197, v56, vcc
	v_cmp_gt_u32_e32 vcc, s71, v119
	v_subrev_u32_e32 v119, 48, v2
	s_nop 0
	v_cndmask_b32_e32 v57, v197, v57, vcc
	v_cmp_gt_u32_e32 vcc, s71, v119
	v_subrev_u32_e32 v119, 49, v2
	s_nop 0
	v_cndmask_b32_e32 v58, v197, v58, vcc
	v_cmp_gt_u32_e32 vcc, s71, v119
	v_subrev_u32_e32 v119, 50, v2
	s_nop 0
	v_cndmask_b32_e32 v59, v197, v59, vcc
	v_cmp_gt_u32_e32 vcc, s71, v119
	v_subrev_u32_e32 v119, 51, v2
	s_nop 0
	v_cndmask_b32_e32 v60, v197, v60, vcc
	v_cmp_gt_u32_e32 vcc, s71, v119
	v_subrev_u32_e32 v119, 56, v2
	s_nop 0
	v_cndmask_b32_e32 v61, v197, v61, vcc
	v_cmp_gt_u32_e32 vcc, s71, v119
	v_subrev_u32_e32 v119, 57, v2
	s_nop 0
	v_cndmask_b32_e32 v62, v197, v62, vcc
	v_cmp_gt_u32_e32 vcc, s71, v119
	v_subrev_u32_e32 v119, 58, v2
	v_subrev_u32_e32 v2, 59, v2
	v_cndmask_b32_e32 v63, v197, v63, vcc
	v_cmp_gt_u32_e32 vcc, s71, v119
	s_nop 1
	v_cndmask_b32_e32 v64, v197, v64, vcc
	v_cmp_gt_u32_e32 vcc, s71, v2
	s_nop 1
	v_cndmask_b32_e32 v65, v197, v65, vcc

.Lring_issue_skip_1:
	s_add_i32 s1, s0, 0x7c0
	s_cmp_gt_i32 s1, s19
	s_cselect_b64 s[28:29], -1, 0
	s_addk_i32 s0, 0x7df
	s_cmp_lt_i32 s0, s20
	s_cselect_b64 s[30:31], -1, 0
	s_or_b64 s[28:29], s[28:29], s[30:31]
	s_and_b64 vcc, exec, s[28:29]
	s_cbranch_vccnz .LBB0_771
	ds_read_b128 v[4:7], v118
	ds_read_b128 v[188:191], v117
	ds_read_b128 v[192:195], v116
	ds_read_b128 v[202:205], v115
	s_and_b32 s1, s1, 0xc0
	v_or_b32_e32 v2, s1, v102
	v_cvt_f32_ubyte0_e32 v2, v2
	v_or_b32_sdwa v2, v2, v114 dst_sel:DWORD dst_unused:UNUSED_PAD src0_sel:DWORD src1_sel:WORD_1
	v_cndmask_b32_e64 v246, 0, v2, s[36:37]
	s_cmp_ge_i32 s16, s0
	s_cselect_b64 s[0:1], -1, 0
	s_waitcnt lgkmcnt(3)
	s_setprio 1
	v_mfma_f32_32x32x16_bf16 v[50:65], v[4:7], v[66:69], 0
	s_cmpk_lt_i32 s15, 0x61
	s_cselect_b64 s[28:29], -1, 0
	s_and_b64 s[0:1], s[0:1], s[28:29]
	s_and_b64 vcc, exec, s[0:1]
	s_waitcnt lgkmcnt(2)
	v_mfma_f32_32x32x16_bf16 v[50:65], v[188:191], v[70:73], v[50:65]
	s_waitcnt lgkmcnt(1)
	v_mfma_f32_32x32x16_bf16 v[50:65], v[192:195], v[74:77], v[50:65]
	s_waitcnt lgkmcnt(0)
	v_mfma_f32_32x32x16_bf16 v[50:65], v[202:205], v[78:81], v[50:65]
	v_mfma_f32_32x32x16_bf16 v[50:65], v[246:249], v[82:85], v[50:65]
	v_add3_u32 v2, v16, v96, s67
	v_add3_u32 v16, v17, v96, s67
	ds_read_b64_tr_b16 v[86:87], v2
	ds_read_b64_tr_b16 v[88:89], v2 offset:1024
	ds_read_b64_tr_b16 v[12:13], v16
	ds_read_b64_tr_b16 v[14:15], v16 offset:1024
	ds_read_b64_tr_b16 v[8:9], v2 offset:2048
	ds_read_b64_tr_b16 v[10:11], v2 offset:3072
	ds_read_b64_tr_b16 v[4:5], v16 offset:2048
	ds_read_b64_tr_b16 v[6:7], v16 offset:3072
	s_cbranch_vccnz .LBB0_791
	v_add_u32_e32 v2, s15, v111
	v_cmp_gt_u32_e32 vcc, s71, v2
	v_add_u32_e32 v16, s17, v112
	s_nop 5
	v_cndmask_b32_e32 v50, v197, v50, vcc
	v_cmp_lt_u32_e32 vcc, s47, v16
	v_add_u32_e32 v16, -2, v2
	s_nop 0
	v_cndmask_b32_e32 v51, v197, v51, vcc
	v_cmp_gt_u32_e32 vcc, s71, v16
	v_add_u32_e32 v16, -3, v2
	s_nop 0
	v_cndmask_b32_e32 v52, v197, v52, vcc
	v_cmp_gt_u32_e32 vcc, s71, v16
	v_add_u32_e32 v16, -8, v2
	s_nop 0
	v_cndmask_b32_e32 v53, v197, v53, vcc
	v_cmp_gt_u32_e32 vcc, s71, v16
	v_add_u32_e32 v16, -9, v2
	s_nop 0
	v_cndmask_b32_e32 v54, v197, v54, vcc
	v_cmp_gt_u32_e32 vcc, s71, v16
	v_add_u32_e32 v16, -10, v2
	s_nop 0
	v_cndmask_b32_e32 v55, v197, v55, vcc
	v_cmp_gt_u32_e32 vcc, s71, v16
	v_add_u32_e32 v16, -11, v2
	s_nop 0
	v_cndmask_b32_e32 v56, v197, v56, vcc
	v_cmp_gt_u32_e32 vcc, s71, v16
	v_add_u32_e32 v16, -16, v2
	s_nop 0
	v_cndmask_b32_e32 v57, v197, v57, vcc
	v_cmp_gt_u32_e32 vcc, s71, v16
	v_subrev_u32_e32 v16, 17, v2
	s_nop 0
	v_cndmask_b32_e32 v58, v197, v58, vcc
	v_cmp_gt_u32_e32 vcc, s71, v16
	v_subrev_u32_e32 v16, 18, v2
	s_nop 0
	v_cndmask_b32_e32 v59, v197, v59, vcc
	v_cmp_gt_u32_e32 vcc, s71, v16
	v_subrev_u32_e32 v16, 19, v2
	s_nop 0
	v_cndmask_b32_e32 v60, v197, v60, vcc
	v_cmp_gt_u32_e32 vcc, s71, v16
	v_subrev_u32_e32 v16, 24, v2
	s_nop 0
	v_cndmask_b32_e32 v61, v197, v61, vcc
	v_cmp_gt_u32_e32 vcc, s71, v16
	v_subrev_u32_e32 v16, 25, v2
	s_nop 0
	v_cndmask_b32_e32 v62, v197, v62, vcc
	v_cmp_gt_u32_e32 vcc, s71, v16
	v_subrev_u32_e32 v16, 26, v2
	v_subrev_u32_e32 v2, 27, v2
	v_cndmask_b32_e32 v63, v197, v63, vcc
	v_cmp_gt_u32_e32 vcc, s71, v16
	s_nop 1
	v_cndmask_b32_e32 v64, v197, v64, vcc
	v_cmp_gt_u32_e32 vcc, s71, v2
	s_nop 1
	v_cndmask_b32_e32 v65, v197, v65, vcc
